# v23: v21 + MLA step-1 row-sum chain moved from the QK/softmax interleave into the P.V stage (bit-identical sums)
# speedup vs baseline: 1.0036x; 1.0036x over previous
.LBB0_946:
	s_sub_i32 s1, s37, 94
	s_cmp_gt_i32 s1, s35
	s_cbranch_scc1 .Lmla_qkskip1
	s_lshl_b32 s50, s0, 14
	s_add_i32 s1, s50, 0
	v_add_u32_e32 v210, s1, v202
	ds_read_b128 v[98:101], v210 offset:49152
	ds_read_b128 v[102:105], v210 offset:57344
	v_xor_b32_e32 v210, 0x80, v210
	v_max_f32_e32 v186, v67, v67
	v_max_f32_e32 v187, v66, v66
	v_max_f32_e32 v186, v187, v186
	s_waitcnt lgkmcnt(1)
	v_mfma_f32_32x32x16_bf16 v[114:129], v[98:101], v[130:133], 0
	v_add_u32_e32 v212, s1, v207
	v_max3_f32 v186, v186, v68, v69
	ds_read_b128 v[178:181], v212 offset:49152
	ds_read_b128 v[182:185], v212 offset:57344
	v_xor_b32_e32 v212, 0x80, v212
	v_max3_f32 v186, v186, v70, v71
	v_max3_f32 v186, v186, v72, v73
	v_max3_f32 v186, v186, v74, v75
	v_max3_f32 v186, v186, v76, v77
	s_waitcnt lgkmcnt(2)
	v_mfma_f32_32x32x16_bf16 v[98:113], v[102:105], v[130:133], 0
	v_max3_f32 v186, v186, v78, v79
	v_lshl_add_u32 v211, s0, 13, v225
	v_max3_f32 v213, v186, v80, v81
	s_waitcnt lgkmcnt(1)
	v_mfma_f32_32x32x16_bf16 v[114:129], v[178:181], v[134:137], v[114:129]
	v_max3_f32 v178, v213, v82, v83
	v_max3_f32 v178, v178, v84, v85
	v_max3_f32 v178, v178, v86, v87
	v_max3_f32 v178, v178, v88, v89
	v_max3_f32 v178, v178, v90, v91
	v_max3_f32 v178, v178, v92, v93
	v_max3_f32 v178, v178, v94, v95
	v_max3_f32 v178, v178, v96, v97
	v_mov_b32_e32 v179, v178
	s_nop 1
	v_permlane32_swap_b32_e32 v178, v179
	v_max_f32_e32 v179, v179, v179
	v_max_f32_e32 v178, v178, v178
	v_max_f32_e32 v178, v178, v179
	v_sub_f32_e32 v179, v178, v231
	v_mul_f32_e32 v179, 0x3d93cd3a, v179
	v_cmp_ge_f32_e32 vcc, s36, v179
	s_cmp_eq_u64 vcc, exec
	v_max_f32_e32 v179, v231, v231
	s_waitcnt lgkmcnt(0)
	v_mfma_f32_32x32x16_bf16 v[98:113], v[182:185], v[134:137], v[98:113]
	s_cselect_b64 vcc, -1, 0
	v_max_f32_e32 v178, v179, v178
	v_cndmask_b32_e32 v232, v178, v231, vcc
	v_add_u32_e32 v218, s1, v209
	v_sub_f32_e32 v178, v231, v232
	ds_read_b128 v[186:189], v218 offset:49152
	ds_read_b128 v[190:193], v218 offset:57344
	v_xor_b32_e32 v218, 0x80, v218
	v_mul_f32_e32 v178, 0x3dd53b94, v178
	v_exp_f32_e32 v231, v178
	v_mul_f32_e32 v213, 0xbdd53b94, v232
	v_fmamk_f32 v66, v66, 0x3dd53b94, v213
	s_waitcnt lgkmcnt(1)
	v_mfma_f32_32x32x16_bf16 v[114:129], v[186:189], v[138:141], v[114:129]
	v_exp_f32_e32 v66, v66
	v_fmamk_f32 v82, v82, 0x3dd53b94, v213
	v_add_u32_e32 v219, s1, v224
	v_exp_f32_e32 v82, v82
	v_fmamk_f32 v67, v67, 0x3dd53b94, v213
	ds_read_b128 v[178:181], v219 offset:49152
	ds_read_b128 v[182:185], v219 offset:57344
	v_xor_b32_e32 v219, 0x80, v219
	v_exp_f32_e32 v67, v67
	s_waitcnt lgkmcnt(2)
	v_mfma_f32_32x32x16_bf16 v[98:113], v[190:193], v[138:141], v[98:113]
	v_fmamk_f32 v83, v83, 0x3dd53b94, v213
	v_exp_f32_e32 v83, v83
	v_fmamk_f32 v68, v68, 0x3dd53b94, v213
	s_waitcnt lgkmcnt(1)
	v_mfma_f32_32x32x16_bf16 v[114:129], v[178:181], v[142:145], v[114:129]
	v_exp_f32_e32 v68, v68
	v_fmamk_f32 v84, v84, 0x3dd53b94, v213
	v_exp_f32_e32 v84, v84
	v_fmamk_f32 v69, v69, 0x3dd53b94, v213
	ds_read_b128 v[186:189], v210 offset:49152
	ds_read_b128 v[190:193], v210 offset:57344
	v_exp_f32_e32 v69, v69
	v_fmamk_f32 v85, v85, 0x3dd53b94, v213
	s_waitcnt lgkmcnt(2)
	v_mfma_f32_32x32x16_bf16 v[98:113], v[182:185], v[142:145], v[98:113]
	v_exp_f32_e32 v85, v85
	v_fmamk_f32 v70, v70, 0x3dd53b94, v213
	s_waitcnt lgkmcnt(1)
	v_mfma_f32_32x32x16_bf16 v[114:129], v[186:189], v[146:149], v[114:129]
	v_exp_f32_e32 v70, v70
	v_fmamk_f32 v86, v86, 0x3dd53b94, v213
	v_exp_f32_e32 v86, v86
	v_fmamk_f32 v71, v71, 0x3dd53b94, v213
	ds_read_b128 v[178:181], v212 offset:49152
	ds_read_b128 v[182:185], v212 offset:57344
	v_exp_f32_e32 v71, v71
	v_fmamk_f32 v87, v87, 0x3dd53b94, v213
	s_waitcnt lgkmcnt(2)
	v_mfma_f32_32x32x16_bf16 v[98:113], v[190:193], v[146:149], v[98:113]
	v_exp_f32_e32 v87, v87
	v_fmamk_f32 v72, v72, 0x3dd53b94, v213
	s_waitcnt lgkmcnt(1)
	v_mfma_f32_32x32x16_bf16 v[114:129], v[178:181], v[150:153], v[114:129]
	v_exp_f32_e32 v72, v72
	v_fmamk_f32 v88, v88, 0x3dd53b94, v213
	v_exp_f32_e32 v88, v88
	v_fmamk_f32 v73, v73, 0x3dd53b94, v213
	ds_read_b128 v[186:189], v218 offset:49152
	ds_read_b128 v[190:193], v218 offset:57344
	v_exp_f32_e32 v73, v73
	v_fmamk_f32 v89, v89, 0x3dd53b94, v213
	s_waitcnt lgkmcnt(2)
	v_mfma_f32_32x32x16_bf16 v[98:113], v[182:185], v[150:153], v[98:113]
	v_exp_f32_e32 v89, v89
	v_fmamk_f32 v74, v74, 0x3dd53b94, v213
	v_exp_f32_e32 v74, v74
	v_fmamk_f32 v90, v90, 0x3dd53b94, v213
	s_waitcnt lgkmcnt(1)
	v_mfma_f32_32x32x16_bf16 v[114:129], v[186:189], v[154:157], v[114:129]
	v_exp_f32_e32 v90, v90
	v_fmamk_f32 v75, v75, 0x3dd53b94, v213
	v_exp_f32_e32 v75, v75
	v_fmamk_f32 v91, v91, 0x3dd53b94, v213
	ds_read_b128 v[178:181], v219 offset:49152
	ds_read_b128 v[182:185], v219 offset:57344
	v_exp_f32_e32 v91, v91
	s_waitcnt lgkmcnt(2)
	v_mfma_f32_32x32x16_bf16 v[98:113], v[190:193], v[154:157], v[98:113]
	v_fmamk_f32 v76, v76, 0x3dd53b94, v213
	v_exp_f32_e32 v76, v76
	v_fmamk_f32 v92, v92, 0x3dd53b94, v213
	s_waitcnt lgkmcnt(1)
	v_mfma_f32_32x32x16_bf16 v[114:129], v[178:181], v[158:161], v[114:129]
	v_exp_f32_e32 v92, v92
	v_fmamk_f32 v77, v77, 0x3dd53b94, v213
	v_add_u32_e32 v186, v211, v226
	v_exp_f32_e32 v77, v77
	v_fmamk_f32 v93, v93, 0x3dd53b94, v213
	ds_read_b128 v[178:181], v186
	ds_read_b128 v[186:189], v186 offset:4096
	v_exp_f32_e32 v93, v93
	s_waitcnt lgkmcnt(2)
	v_mfma_f32_32x32x16_bf16 v[98:113], v[182:185], v[158:161], v[98:113]
	v_fmamk_f32 v78, v78, 0x3dd53b94, v213
	v_exp_f32_e32 v78, v78
	v_fmamk_f32 v94, v94, 0x3dd53b94, v213
	s_waitcnt lgkmcnt(1)
	v_mfma_f32_32x32x16_bf16 v[114:129], v[178:181], v[162:165], v[114:129]
	v_exp_f32_e32 v94, v94
	v_fmamk_f32 v79, v79, 0x3dd53b94, v213
	v_add_u32_e32 v182, v211, v206
	v_exp_f32_e32 v79, v79
	v_fmamk_f32 v95, v95, 0x3dd53b94, v213
	ds_read_b128 v[178:181], v182
	ds_read_b128 v[182:185], v182 offset:4096
	v_exp_f32_e32 v95, v95
	s_waitcnt lgkmcnt(2)
	v_mfma_f32_32x32x16_bf16 v[98:113], v[186:189], v[162:165], v[98:113]
	v_fmamk_f32 v80, v80, 0x3dd53b94, v213
	v_exp_f32_e32 v80, v80
	v_fmamk_f32 v96, v96, 0x3dd53b94, v213
	s_waitcnt lgkmcnt(1)
	v_mfma_f32_32x32x16_bf16 v[114:129], v[178:181], v[166:169], v[114:129]
	v_exp_f32_e32 v96, v96
	v_fmamk_f32 v81, v81, 0x3dd53b94, v213
	v_add_u32_e32 v186, v211, v208
	v_exp_f32_e32 v81, v81
	v_fmac_f32_e32 v213, 0x3dd53b94, v97
	ds_read_b128 v[178:181], v186
	ds_read_b128 v[186:189], v186 offset:4096
	v_exp_f32_e32 v97, v213
	s_waitcnt lgkmcnt(2)
	v_mfma_f32_32x32x16_bf16 v[98:113], v[182:185], v[166:169], v[98:113]
	s_waitcnt lgkmcnt(1)
	v_mfma_f32_32x32x16_bf16 v[114:129], v[178:181], v[170:173], v[114:129]
	v_add_u32_e32 v182, v211, v223
	ds_read_b128 v[190:193], v182
	ds_read_b128 v[236:239], v182 offset:4096
	v_cvt_pk_bf16_f32 v178, v66, v67
	v_cvt_pk_bf16_f32 v179, v68, v69
	v_cvt_pk_bf16_f32 v180, v70, v71
	v_cvt_pk_bf16_f32 v181, v72, v73
	s_waitcnt lgkmcnt(2)
	v_mfma_f32_32x32x16_bf16 v[98:113], v[186:189], v[170:173], v[98:113]
	v_cvt_pk_bf16_f32 v182, v74, v75
	v_cvt_pk_bf16_f32 v183, v76, v77
	v_cvt_pk_bf16_f32 v184, v78, v79
	v_cvt_pk_bf16_f32 v185, v80, v81
	v_permlane32_swap_b32_e32 v178, v180
	v_permlane32_swap_b32_e32 v179, v181
	v_permlane32_swap_b32_e32 v182, v184
	v_permlane32_swap_b32_e32 v183, v185
	s_waitcnt lgkmcnt(1)
	v_mfma_f32_32x32x16_bf16 v[114:129], v[190:193], v[174:177], v[114:129]
	v_cvt_pk_bf16_f32 v186, v82, v83
	v_cvt_pk_bf16_f32 v187, v84, v85
	v_cvt_pk_bf16_f32 v188, v86, v87
	v_cvt_pk_bf16_f32 v189, v88, v89
	v_cvt_pk_bf16_f32 v190, v90, v91
	v_cvt_pk_bf16_f32 v191, v92, v93
	v_cvt_pk_bf16_f32 v192, v94, v95
	s_waitcnt lgkmcnt(0)
	v_mfma_f32_32x32x16_bf16 v[98:113], v[236:239], v[174:177], v[98:113]
	v_cvt_pk_bf16_f32 v193, v96, v97
	v_permlane32_swap_b32_e32 v186, v188
	v_permlane32_swap_b32_e32 v187, v189
	v_permlane32_swap_b32_e32 v190, v192
	v_permlane32_swap_b32_e32 v191, v193

.LBB0_950:
	s_sub_i32 s1, s37, 0x9e
	s_cmp_gt_i32 s1, s35
	s_cbranch_scc1 .Lmla_pvskip1
	s_lshl_b32 s0, s40, 14
	v_add_u32_e32 v210, s0, v228
	ds_read_b64_tr_b16 v[218:219], v210 offset:0
	ds_read_b64_tr_b16 v[220:221], v210 offset:0x800
	ds_read_b64_tr_b16 v[236:237], v210 offset:0x1000
	ds_read_b64_tr_b16 v[238:239], v210 offset:0x1800
	ds_read_b64_tr_b16 v[240:241], v210 offset:0x2000
	ds_read_b64_tr_b16 v[242:243], v210 offset:0x2800
	ds_read_b64_tr_b16 v[244:245], v210 offset:0x3000
	ds_read_b64_tr_b16 v[246:247], v210 offset:0x3800
	s_waitcnt lgkmcnt(0)
	s_nop 0
	v_mfma_f32_32x32x16_bf16 v[50:65], v[178:181], v[218:221], v[50:65]
	v_add_f32_e32 v233, v66, v82
	v_add_f32_e32 v233, v67, v233
	ds_read_b64_tr_b16 v[218:219], v210 offset:0x200
	ds_read_b64_tr_b16 v[220:221], v210 offset:0xa00
	v_mfma_f32_32x32x16_bf16 v[50:65], v[182:185], v[236:239], v[50:65]
	v_add_f32_e32 v233, v83, v233
	v_add_f32_e32 v233, v68, v233
	ds_read_b64_tr_b16 v[236:237], v210 offset:0x1200
	ds_read_b64_tr_b16 v[238:239], v210 offset:0x1a00
	v_mfma_f32_32x32x16_bf16 v[50:65], v[186:189], v[240:243], v[50:65]
	v_add_f32_e32 v233, v84, v233
	v_add_f32_e32 v233, v69, v233
	ds_read_b64_tr_b16 v[240:241], v210 offset:0x2200
	ds_read_b64_tr_b16 v[242:243], v210 offset:0x2a00
	v_mfma_f32_32x32x16_bf16 v[50:65], v[190:193], v[244:247], v[50:65]
	v_add_f32_e32 v233, v85, v233
	v_add_f32_e32 v233, v70, v233
	ds_read_b64_tr_b16 v[244:245], v210 offset:0x3200
	ds_read_b64_tr_b16 v[246:247], v210 offset:0x3a00
	s_waitcnt lgkmcnt(0)
	v_mfma_f32_32x32x16_bf16 v[34:49], v[178:181], v[218:221], v[34:49]
	v_add_f32_e32 v233, v86, v233
	v_add_f32_e32 v233, v71, v233
	ds_read_b64_tr_b16 v[218:219], v210 offset:0x400
	ds_read_b64_tr_b16 v[220:221], v210 offset:0xc00
	v_mfma_f32_32x32x16_bf16 v[34:49], v[182:185], v[236:239], v[34:49]
	v_add_f32_e32 v233, v87, v233
	v_add_f32_e32 v233, v72, v233
	ds_read_b64_tr_b16 v[236:237], v210 offset:0x1400
	ds_read_b64_tr_b16 v[238:239], v210 offset:0x1c00
	v_mfma_f32_32x32x16_bf16 v[34:49], v[186:189], v[240:243], v[34:49]
	v_add_f32_e32 v233, v88, v233
	v_add_f32_e32 v233, v73, v233
	ds_read_b64_tr_b16 v[240:241], v210 offset:0x2400
	ds_read_b64_tr_b16 v[242:243], v210 offset:0x2c00
	v_mfma_f32_32x32x16_bf16 v[34:49], v[190:193], v[244:247], v[34:49]
	v_add_f32_e32 v233, v89, v233
	v_add_f32_e32 v233, v74, v233
	ds_read_b64_tr_b16 v[244:245], v210 offset:0x3400
	ds_read_b64_tr_b16 v[246:247], v210 offset:0x3c00
	s_waitcnt lgkmcnt(0)
	v_mfma_f32_32x32x16_bf16 v[18:33], v[178:181], v[218:221], v[18:33]
	v_add_f32_e32 v233, v90, v233
	v_add_f32_e32 v233, v75, v233
	ds_read_b64_tr_b16 v[218:219], v210 offset:0x600
	ds_read_b64_tr_b16 v[220:221], v210 offset:0xe00
	v_mfma_f32_32x32x16_bf16 v[18:33], v[182:185], v[236:239], v[18:33]
	v_add_f32_e32 v233, v91, v233
	v_add_f32_e32 v233, v76, v233
	ds_read_b64_tr_b16 v[236:237], v210 offset:0x1600
	ds_read_b64_tr_b16 v[238:239], v210 offset:0x1e00
	v_mfma_f32_32x32x16_bf16 v[18:33], v[186:189], v[240:243], v[18:33]
	v_add_f32_e32 v233, v92, v233
	v_add_f32_e32 v233, v77, v233
	ds_read_b64_tr_b16 v[240:241], v210 offset:0x2600
	ds_read_b64_tr_b16 v[242:243], v210 offset:0x2e00
	v_mfma_f32_32x32x16_bf16 v[18:33], v[190:193], v[244:247], v[18:33]
	v_add_f32_e32 v233, v93, v233
	v_add_f32_e32 v233, v78, v233
	ds_read_b64_tr_b16 v[244:245], v210 offset:0x3600
	ds_read_b64_tr_b16 v[246:247], v210 offset:0x3e00
	s_waitcnt lgkmcnt(0)
	v_mfma_f32_32x32x16_bf16 v[2:17], v[178:181], v[218:221], v[2:17]
	v_add_f32_e32 v233, v94, v233
	v_add_f32_e32 v233, v79, v233
	s_waitcnt vmcnt(0)
	s_cmp_ge_u32 s34, s21
	s_barrier
	v_mfma_f32_32x32x16_bf16 v[2:17], v[182:185], v[236:239], v[2:17]
	v_add_f32_e32 v233, v95, v233
	v_add_f32_e32 v233, v80, v233
	v_mfma_f32_32x32x16_bf16 v[2:17], v[186:189], v[240:243], v[2:17]
	v_add_f32_e32 v233, v96, v233
	v_add_f32_e32 v233, v81, v233
	v_mfma_f32_32x32x16_bf16 v[2:17], v[190:193], v[244:247], v[2:17]
	v_add_f32_e32 v233, v97, v233
	v_mov_b32_e32 v234, v233
	s_nop 1
	v_permlane32_swap_b32_e32 v233, v234

.Lmla_qkskip1:
	s_lshl_b32 s50, s0, 14
	s_add_i32 s1, s50, 0
	v_add_u32_e32 v210, s1, v202
	v_xor_b32_e32 v210, 0x80, v210
	v_max_f32_e32 v186, v67, v67
	v_max_f32_e32 v187, v66, v66
	v_max_f32_e32 v186, v187, v186
	v_add_u32_e32 v212, s1, v207
	v_max3_f32 v186, v186, v68, v69
	v_xor_b32_e32 v212, 0x80, v212
	v_max3_f32 v186, v186, v70, v71
	v_max3_f32 v186, v186, v72, v73
	v_max3_f32 v186, v186, v74, v75
	v_max3_f32 v186, v186, v76, v77
	v_max3_f32 v186, v186, v78, v79
	v_lshl_add_u32 v211, s0, 13, v225
	v_max3_f32 v213, v186, v80, v81
	v_max3_f32 v178, v213, v82, v83
	v_max3_f32 v178, v178, v84, v85
	v_max3_f32 v178, v178, v86, v87
	v_max3_f32 v178, v178, v88, v89
	v_max3_f32 v178, v178, v90, v91
	v_max3_f32 v178, v178, v92, v93
	v_max3_f32 v178, v178, v94, v95
	v_max3_f32 v178, v178, v96, v97
	v_mov_b32_e32 v179, v178
	s_nop 1
	v_permlane32_swap_b32_e32 v178, v179
	v_max_f32_e32 v179, v179, v179
	v_max_f32_e32 v178, v178, v178
	v_max_f32_e32 v178, v178, v179
	v_sub_f32_e32 v179, v178, v231
	v_mul_f32_e32 v179, 0x3d93cd3a, v179
	v_cmp_ge_f32_e32 vcc, s36, v179
	s_cmp_eq_u64 vcc, exec
	v_max_f32_e32 v179, v231, v231
	s_cselect_b64 vcc, -1, 0
	v_max_f32_e32 v178, v179, v178
	v_cndmask_b32_e32 v232, v178, v231, vcc
	v_add_u32_e32 v218, s1, v209
	v_sub_f32_e32 v178, v231, v232
	v_xor_b32_e32 v218, 0x80, v218
	v_mul_f32_e32 v178, 0x3dd53b94, v178
	v_exp_f32_e32 v231, v178
	v_mul_f32_e32 v213, 0xbdd53b94, v232
	v_fmamk_f32 v66, v66, 0x3dd53b94, v213
	v_exp_f32_e32 v66, v66
	v_fmamk_f32 v82, v82, 0x3dd53b94, v213
	v_add_u32_e32 v219, s1, v224
	v_exp_f32_e32 v82, v82
	v_fmamk_f32 v67, v67, 0x3dd53b94, v213
	v_xor_b32_e32 v219, 0x80, v219
	v_exp_f32_e32 v67, v67
	v_fmamk_f32 v83, v83, 0x3dd53b94, v213
	v_exp_f32_e32 v83, v83
	v_fmamk_f32 v68, v68, 0x3dd53b94, v213
	v_exp_f32_e32 v68, v68
	v_fmamk_f32 v84, v84, 0x3dd53b94, v213
	v_exp_f32_e32 v84, v84
	v_fmamk_f32 v69, v69, 0x3dd53b94, v213
	v_exp_f32_e32 v69, v69
	v_fmamk_f32 v85, v85, 0x3dd53b94, v213
	v_exp_f32_e32 v85, v85
	v_fmamk_f32 v70, v70, 0x3dd53b94, v213
	v_exp_f32_e32 v70, v70
	v_fmamk_f32 v86, v86, 0x3dd53b94, v213
	v_exp_f32_e32 v86, v86
	v_fmamk_f32 v71, v71, 0x3dd53b94, v213
	v_exp_f32_e32 v71, v71
	v_fmamk_f32 v87, v87, 0x3dd53b94, v213
	v_exp_f32_e32 v87, v87
	v_fmamk_f32 v72, v72, 0x3dd53b94, v213
	v_exp_f32_e32 v72, v72
	v_fmamk_f32 v88, v88, 0x3dd53b94, v213
	v_exp_f32_e32 v88, v88
	v_fmamk_f32 v73, v73, 0x3dd53b94, v213
	v_exp_f32_e32 v73, v73
	v_fmamk_f32 v89, v89, 0x3dd53b94, v213
	v_exp_f32_e32 v89, v89
	v_fmamk_f32 v74, v74, 0x3dd53b94, v213
	v_exp_f32_e32 v74, v74
	v_fmamk_f32 v90, v90, 0x3dd53b94, v213
	v_exp_f32_e32 v90, v90
	v_fmamk_f32 v75, v75, 0x3dd53b94, v213
	v_exp_f32_e32 v75, v75
	v_fmamk_f32 v91, v91, 0x3dd53b94, v213
	v_exp_f32_e32 v91, v91
	v_fmamk_f32 v76, v76, 0x3dd53b94, v213
	v_exp_f32_e32 v76, v76
	v_fmamk_f32 v92, v92, 0x3dd53b94, v213
	v_exp_f32_e32 v92, v92
	v_fmamk_f32 v77, v77, 0x3dd53b94, v213
	v_add_u32_e32 v186, v211, v226
	v_exp_f32_e32 v77, v77
	v_fmamk_f32 v93, v93, 0x3dd53b94, v213
	v_exp_f32_e32 v93, v93
	v_fmamk_f32 v78, v78, 0x3dd53b94, v213
	v_exp_f32_e32 v78, v78
	v_fmamk_f32 v94, v94, 0x3dd53b94, v213
	v_exp_f32_e32 v94, v94
	v_fmamk_f32 v79, v79, 0x3dd53b94, v213
	v_add_u32_e32 v182, v211, v206
	v_exp_f32_e32 v79, v79
	v_fmamk_f32 v95, v95, 0x3dd53b94, v213
	v_exp_f32_e32 v95, v95
	v_fmamk_f32 v80, v80, 0x3dd53b94, v213
	v_exp_f32_e32 v80, v80
	v_fmamk_f32 v96, v96, 0x3dd53b94, v213
	v_exp_f32_e32 v96, v96
	v_fmamk_f32 v81, v81, 0x3dd53b94, v213
	v_add_u32_e32 v186, v211, v208
	v_exp_f32_e32 v81, v81
	v_fmac_f32_e32 v213, 0x3dd53b94, v97
	v_exp_f32_e32 v97, v213
	v_add_u32_e32 v182, v211, v223
	v_cvt_pk_bf16_f32 v178, v66, v67
	v_cvt_pk_bf16_f32 v179, v68, v69
	v_cvt_pk_bf16_f32 v180, v70, v71
	v_cvt_pk_bf16_f32 v181, v72, v73
	v_cvt_pk_bf16_f32 v182, v74, v75
	v_cvt_pk_bf16_f32 v183, v76, v77
	v_cvt_pk_bf16_f32 v184, v78, v79
	v_cvt_pk_bf16_f32 v185, v80, v81
	v_permlane32_swap_b32_e32 v178, v180
	v_permlane32_swap_b32_e32 v179, v181
	v_permlane32_swap_b32_e32 v182, v184
	v_permlane32_swap_b32_e32 v183, v185
	v_cvt_pk_bf16_f32 v186, v82, v83
	v_cvt_pk_bf16_f32 v187, v84, v85
	v_cvt_pk_bf16_f32 v188, v86, v87
	v_cvt_pk_bf16_f32 v189, v88, v89
	v_cvt_pk_bf16_f32 v190, v90, v91
	v_cvt_pk_bf16_f32 v191, v92, v93
	v_cvt_pk_bf16_f32 v192, v94, v95
	v_cvt_pk_bf16_f32 v193, v96, v97
	v_permlane32_swap_b32_e32 v186, v188
	v_permlane32_swap_b32_e32 v187, v189
	v_permlane32_swap_b32_e32 v190, v192
	v_permlane32_swap_b32_e32 v191, v193
	s_branch .Lmla_qk1_join
